# phase-start de-serialisation for the in-proj and out-proj GEMMs: row-statistics wait + 1/rms compute + table writes moved behind the issue of the first-tile LDS-DMA loads (two cold round trips overlap
# speedup vs baseline: 1.0042x; 1.0015x over previous
; __device__ __forceinline__ int launder_v(int v) { asm volatile("" : "+v"(v)); return v; }
; __device__ __forceinline__ float rsq_(float x) { return 1.0f / sqrtf(x); }
; #define PG8_STAGEB(bufoff, gbase) do { _Pragma("unroll") for (int _i = 0; _i < 2; ++_i) PG8_GL((const char*)(gbase) + voffB[_i], bufoff, _i); } while (0)
; #define PG8_STAGEA(bufoff, ubase, offs, h, kb) do { _Pragma("unroll") for (int _i = 0; _i < 2; ++_i) { \
;         if constexpr (P::GATHER) PG8_GL(S.A + (size_t)(kb) + (offs)[h][_i], bufoff, _i); \
;         else PG8_GL((const char*)(ubase) + (size_t)(h) * hstepA + (size_t)(kb) + voffA[_i], bufoff, _i); } } while (0)
; #define PG8_WAIT_V(n) asm volatile("s_waitcnt vmcnt(" #n ")" ::: "memory")
; #define PG8_BAR __builtin_amdgcn_s_barrier()
; __device__ __forceinline__ LAS float* T0(ldsp tab, int par) { return (LAS float*)(tab) + par * 256; }
; __device__ __forceinline__ LAS float* T3(ldsp tab, int par) { return (LAS float*)(tab + 6144) + par * 512; }
; #define PROB_WS() unsigned char* w_ = ws; asm volatile("" : "+s"(w_))
; template <class P, bool ALIGN_EPI>
; __device__ __forceinline__ void gemm_phase(ldsp lds, ldsp tab, const P& S) {
;     ...
;     S.prepare(cur, 0, tab);
;     PG8_STAGEB(PG8_SB(0, 0), cB); PG8_STAGEB(PG8_SB(0, 1), cB + hstepB); PG8_STAGEA(PG8_SA(0, 0), cA, goc, 0, 0); PG8_STAGEA(PG8_SA(0, 1), cA, goc, 1, 0);
;     if (wr == 1) PG8_BAR;
;     PG8_WAIT_V(2); PG8_BAR;
;     PG8_STAGEB(PG8_SB(1, 0), cB + kstep); PG8_STAGEA(PG8_SA(1, 0), cA, goc, 0, kstep); PG8_STAGEB(PG8_SB(1, 1), cB + hstepB + kstep);
;     PG8_WAIT_V(6); PG8_BAR;
;     __device__ __forceinline__ void prepare(const Unit& u, int par, ldsp tab) const {
;         PROB_WS(); const float* ssqx = (const float*)(w_ + WS_SSQX);
;         const int tid = launder_v(threadIdx.x); if (tid < 256) { const int row = u.pm * 256 + tid; const float bvl = ((const float*)(w_ + WS_BIN))[((size_t)l * 2 + (u.pm >> 5)) * INP + u.pn * 256 + tid];
;             T0(tab, par)[tid] = rsq_(sum16(ssqx + (size_t)row * 16) * (1.0f / 1024.0f) + EPS); T3(tab, par)[tid] = bvl; } }
.LBB0_832:
	s_andn2_b64 vcc, exec, s[0:1]
	s_cbranch_vccnz .LBB0_932
	s_mov_b64 s[0:1], s[4:5]
	s_waitcnt lgkmcnt(0)
	v_mov_b32_e32 v4, v0
	s_movk_i32 s3, 0x100
	s_lshl_b32 s29, s26, 14
	s_nop 0
	v_cmp_gt_i32_e32 vcc, s3, v4
	s_and_saveexec_b64 s[6:7], vcc
	s_cbranch_execz .LBB0_835
	v_lshl_add_u32 v6, s40, 8, v4
	v_ashrrev_i32_e32 v7, 31, v6
	v_lshlrev_b64 v[6:7], 6, v[6:7]
	v_lshl_add_u64 v[10:11], s[0:1], 0, v[6:7]
	s_mov_b32 s3, 0x364000
	v_add_co_u32_e32 v6, vcc, s3, v10
	s_mov_b64 s[10:11], 0x364000
	s_nop 0
	v_addc_co_u32_e32 v7, vcc, 0, v11, vcc
	global_load_dwordx4 v[26:29], v[6:7], off
	v_lshl_add_u64 v[10:11], v[10:11], 0, s[10:11]
	global_load_dwordx4 v[14:17], v[10:11], off offset:16
	global_load_dwordx4 v[18:21], v[10:11], off offset:32
	global_load_dwordx4 v[22:25], v[10:11], off offset:48
	s_ashr_i32 s10, s40, 5
	s_lshl_b32 s12, s22, 8
	s_ashr_i32 s11, s10, 31
	s_ashr_i32 s13, s12, 31
	s_add_u32 s3, s0, s29
	s_addc_u32 s14, s1, 0
	s_lshl_b64 s[0:1], s[10:11], 13
	s_add_u32 s3, s3, s0
	s_addc_u32 s10, s14, s1
	s_lshl_b64 s[0:1], s[12:13], 2
	s_add_u32 s0, s3, s0
	v_ashrrev_i32_e32 v5, 31, v4
	s_addc_u32 s1, s10, s1
	v_lshl_add_u64 v[10:11], v[4:5], 2, s[0:1]
	s_mov_b32 s0, 0x260000
	v_add_co_u32_e32 v10, vcc, s0, v10
	s_nop 0
	v_addc_co_u32_e32 v11, vcc, 0, v11, vcc
	flat_load_dword v30, v[10:11]
	v_lshl_add_u32 v31, v4, 2, 0
.LBB0_835:
	s_or_b64 exec, exec, s[6:7]
	v_bfe_i32 v4, v12, 27, 1
	v_lshlrev_b32_e32 v1, 4, v12
	v_lshrrev_b32_e32 v4, 22, v4
	s_add_u32 s50, s4, 0x1d0f4000
	v_add_u32_e32 v4, v1, v4
	s_addc_u32 s51, s5, 0
	s_lshl_b32 s0, s26, 22
	v_and_b32_e32 v4, 0xfffffc00, v4
	s_add_u32 s0, s4, s0
	v_sub_u32_e32 v4, v1, v4
	s_addc_u32 s1, s5, 0
	v_ashrrev_i32_e32 v2, 31, v12
	v_lshrrev_b32_e32 v5, 4, v4
	s_add_u32 s52, s0, 0x774000
	v_lshrrev_b32_e32 v2, 26, v2
	v_bitop3_b32 v4, v5, v4, 32 bitop3:0x6c
	s_addc_u32 s53, s1, 0
	s_ashr_i32 s41, s40, 31
	v_add_u32_e32 v2, v12, v2
	v_ashrrev_i32_e32 v6, 31, v4
	s_lshl_b64 s[0:1], s[40:41], 19
	v_ashrrev_i32_e32 v2, 6, v2
	v_lshrrev_b32_e32 v6, 26, v6
	s_add_u32 s0, s50, s0
	v_lshlrev_b32_e32 v5, 3, v2
	v_add_u32_e32 v6, v4, v6
	s_addc_u32 s1, s51, s1
	s_ashr_i32 s23, s22, 31
	v_and_b32_e32 v5, -16, v5
	v_ashrrev_i32_e32 v7, 6, v6
	v_and_b32_e32 v6, 0xc0, v6
	s_lshl_b64 s[6:7], s[22:23], 19
	v_add_u32_e32 v5, v7, v5
	v_sub_u32_e32 v4, v4, v6
	s_add_u32 s30, s52, s6
	v_lshlrev_b32_e32 v2, 5, v2
	v_ashrrev_i16_sdwa v4, v248, sext(v4) dst_sel:DWORD dst_unused:UNUSED_PAD src0_sel:DWORD src1_sel:BYTE_0
	v_lshlrev_b32_e32 v6, 1, v5
	v_lshrrev_b32_e32 v8, 2, v5
	v_and_b32_e32 v7, 3, v7
	s_mov_b32 s6, 0x1fffe0
	v_and_b32_e32 v2, 32, v2
	v_bfe_i32 v4, v4, 0, 16
	v_and_b32_e32 v6, 24, v6
	v_and_b32_e32 v8, 4, v8
	v_and_or_b32 v7, v5, s6, v7
	v_or3_b32 v6, v7, v8, v6
	v_add_lshl_u32 v4, v2, v4, 1
	v_add_u32_e32 v1, 0x2000, v1
	v_lshl_add_u32 v2, v5, 11, v4
	v_lshl_add_u32 v216, v6, 11, v4
	v_ashrrev_i32_e32 v4, 31, v1
	v_lshrrev_b32_e32 v4, 22, v4
	v_add_u32_e32 v4, v1, v4
	v_ashrrev_i32_e32 v4, 10, v4
	v_mul_i32_i24_e32 v5, 0x400, v4
	v_sub_u32_e32 v1, v1, v5
	v_lshrrev_b32_e32 v5, 4, v1
	v_bitop3_b32 v1, v5, v1, 32 bitop3:0x6c
	v_ashrrev_i32_e32 v6, 31, v1
	v_lshrrev_b32_e32 v6, 26, v6
	v_lshlrev_b32_e32 v5, 3, v4
	v_add_u32_e32 v6, v1, v6
	s_addc_u32 s31, s53, s7
	s_ashr_i32 s3, s2, 6
	v_and_b32_e32 v5, -16, v5
	v_ashrrev_i32_e32 v7, 6, v6
	v_and_b32_e32 v6, 0xc0, v6
	v_add_u32_e32 v5, v7, v5
	v_sub_u32_e32 v1, v1, v6
	s_lshl_b32 s54, s3, 10
	v_lshlrev_b32_e32 v4, 5, v4
	v_ashrrev_i16_sdwa v1, v248, sext(v1) dst_sel:DWORD dst_unused:UNUSED_PAD src0_sel:DWORD src1_sel:BYTE_0
	v_lshlrev_b32_e32 v6, 1, v5
	v_lshrrev_b32_e32 v8, 2, v5
	v_and_b32_e32 v7, 3, v7
	s_add_i32 s55, s54, 0
	v_and_b32_e32 v4, 32, v4
	v_bfe_i32 v1, v1, 0, 16
	v_and_b32_e32 v6, 24, v6
	v_and_b32_e32 v8, 4, v8
	v_and_or_b32 v7, v5, s6, v7
	s_add_i32 m0, s55, 0x10000
	v_or3_b32 v6, v7, v8, v6
	v_add_lshl_u32 v1, v4, v1, 1
	s_ashr_i32 s10, s2, 8
	global_load_lds_dwordx4 v216, s[30:31]
	s_add_i32 m0, s55, 0x12000
	v_lshl_add_u32 v220, v6, 11, v1
	s_add_u32 s6, s30, 0x40000
	global_load_lds_dwordx4 v220, s[30:31]
	s_addc_u32 s7, s31, 0
	s_add_i32 m0, s55, 0x14000
	s_add_i32 s56, s55, 0x2000
	global_load_lds_dwordx4 v216, s[6:7]
	s_add_i32 m0, s55, 0x16000
	v_lshl_add_u32 v218, v5, 11, v1
	global_load_lds_dwordx4 v220, s[6:7]
	s_mov_b32 m0, s55
	s_add_u32 s6, s0, 0x40000
	global_load_lds_dwordx4 v2, s[0:1]
	s_mov_b32 m0, s56
	s_addc_u32 s7, s1, 0
	s_add_i32 s57, s55, 0x4000
	global_load_lds_dwordx4 v218, s[0:1]
	s_mov_b32 m0, s57
	s_add_i32 s58, s55, 0x6000
	global_load_lds_dwordx4 v2, s[6:7]
	s_mov_b32 m0, s58
	v_mov_b32_e32 v217, v3
	global_load_lds_dwordx4 v218, s[6:7]
	v_cmp_gt_i32_e32 vcc, 0x100, v0
	s_and_b64 exec, exec, vcc
	s_cbranch_execz .Lprep_inproj_skip
	s_mov_b32 s6, 0xf800000
	s_waitcnt vmcnt(8)
	v_add_f32_e32 v32, v26, v27
	v_add_f32_e32 v5, v28, v29
	v_add_f32_e32 v6, v14, v15
	v_add_f32_e32 v7, v16, v17
	v_add_f32_e32 v8, v18, v19
	v_add_f32_e32 v9, v20, v21
	v_add_f32_e32 v32, v32, v5
	v_add_f32_e32 v5, v6, v7
	v_add_f32_e32 v10, v22, v23
	v_add_f32_e32 v11, v24, v25
	v_add_f32_e32 v6, v8, v9
	v_add_f32_e32 v32, v32, v5
	v_add_f32_e32 v7, v10, v11
	v_add_f32_e32 v32, v32, v6
	v_add_f32_e32 v32, v32, v7
	v_fmamk_f32 v32, v32, 0x3a800000, v247
	v_mul_f32_e32 v5, 0x4f800000, v32
	v_cmp_gt_f32_e32 vcc, s6, v32
	v_add_u32_e32 v6, 0x20000, v31
	v_add_u32_e32 v4, 0x21800, v31
	v_cndmask_b32_e32 v32, v32, v5, vcc
	v_sqrt_f32_e32 v5, v32
	s_nop 0
	v_add_u32_e32 v7, -1, v5
	v_add_u32_e32 v8, 1, v5
	v_fma_f32 v9, -v7, v5, v32
	v_fma_f32 v10, -v8, v5, v32
	v_cmp_ge_f32_e64 s[6:7], 0, v9
	s_nop 1
	v_cndmask_b32_e64 v5, v5, v7, s[6:7]
	v_cmp_lt_f32_e64 s[6:7], 0, v10
	s_nop 1
	v_cndmask_b32_e64 v5, v5, v8, s[6:7]
	v_mul_f32_e32 v7, 0x37800000, v5
	v_cndmask_b32_e32 v5, v5, v7, vcc
	v_cmp_class_f32_e32 vcc, v32, v242
	s_nop 1
	v_cndmask_b32_e32 v32, v5, v32, vcc
	v_div_scale_f32 v5, s[6:7], v32, v32, 1.0
	v_rcp_f32_e32 v7, v5
	v_div_scale_f32 v8, vcc, 1.0, v32, 1.0
	v_fma_f32 v9, -v5, v7, 1.0
	v_fmac_f32_e32 v7, v9, v7
	v_mul_f32_e32 v9, v8, v7
	v_fma_f32 v10, -v5, v9, v8
	v_fmac_f32_e32 v9, v10, v7
	v_fma_f32 v5, -v5, v9, v8
	v_div_fmas_f32 v5, v5, v7, v9
	v_div_fixup_f32 v32, v5, v32, 1.0
	ds_write_b32 v6, v32
	s_waitcnt lgkmcnt(0)
	ds_write_b32 v4, v30
.Lprep_inproj_skip:
	s_mov_b64 exec, -1
	v_mov_b32_e32 v221, v3
	v_mov_b32_e32 v219, v3
	s_cmp_eq_u32 s10, 1
	v_lshl_add_u64 v[10:11], s[30:31], 0, v[216:217]
	s_waitcnt vmcnt(0)
	v_lshl_add_u64 v[8:9], s[30:31], 0, v[220:221]
	v_lshl_add_u64 v[4:5], s[0:1], 0, v[2:3]
	s_cselect_b64 s[6:7], -1, 0
	s_cmp_lg_u32 s10, 1
	v_lshl_add_u64 v[6:7], s[0:1], 0, v[218:219]
	s_cbranch_scc1 .LBB0_837
	s_barrier

; __device__ __forceinline__ int launder_v(int v) { asm volatile("" : "+v"(v)); return v; }
; __device__ __forceinline__ float rsq_(float x) { return 1.0f / sqrtf(x); }
; __device__ __forceinline__ LAS float* T0(ldsp tab, int par) { return (LAS float*)(tab) + par * 256; }
; __device__ __forceinline__ LAS float* T1(ldsp tab, int par) { return (LAS float*)(tab + 2048) + par * 256; }
; #define PROB_WS() unsigned char* w_ = ws; asm volatile("" : "+s"(w_))
;     __device__ __forceinline__ void prepare(const Unit& u, int par, ldsp tab) const {
;         PROB_WS(); const float* ssqo = (const float*)(w_ + WS_SSQO);
;         const int tid = launder_v(threadIdx.x); if (tid < 256) { const float* p = ssqo + ((size_t)u.pm * 256 + tid) * 16; const f32x4 a = gld4(p), b = gld4(p + 4), c = gld4(p + 8), d = gld4(p + 12);
;             const float sm = ((a[0] + a[1]) + (a[2] + a[3])) + ((b[0] + b[1]) + (b[2] + b[3])), ss = ((c[0] + c[1]) + (c[2] + c[3])) + ((d[0] + d[1]) + (d[2] + d[3]));
;             const float rm = rsq_(sm * (1.0f / 512.0f) + EPS), rsb = rsq_(ss * (1.0f / 512.0f) + EPS);
;             T0(tab, par)[tid] = rsb; T1(tab, par)[tid] = rm / rsb; } }
.LBB0_1260:
	s_andn2_b64 vcc, exec, s[0:1]
	s_cbranch_vccnz .LBB0_1414
	s_mov_b64 s[0:1], s[6:7]
	s_waitcnt lgkmcnt(0)
	v_mov_b32_e32 v4, v0
	s_movk_i32 s3, 0x100
	s_ashr_i32 s21, s20, 31
	s_nop 0
	v_cmp_gt_i32_e32 vcc, s3, v4
	s_and_saveexec_b64 s[10:11], vcc
	s_cbranch_execz .LBB0_1263
	s_lshl_b64 s[12:13], s[20:21], 14
	v_ashrrev_i32_e32 v5, 31, v4
	s_add_u32 s0, s0, s12
	s_addc_u32 s1, s1, s13
	v_lshlrev_b64 v[6:7], 6, v[4:5]
	v_lshl_add_u64 v[6:7], s[0:1], 0, v[6:7]
	s_mov_b64 s[0:1], 0x4e4000
	v_lshl_add_u64 v[10:11], v[6:7], 0, s[0:1]
	v_add_co_u32_e32 v6, vcc, 0x4e4000, v6
	s_mov_b32 s3, 0xf800000
	s_nop 0
	v_addc_co_u32_e32 v7, vcc, 0, v7, vcc
	global_load_dwordx4 v[26:29], v[6:7], off
	s_nop 0
	global_load_dwordx4 v[14:17], v[10:11], off offset:48
	global_load_dwordx4 v[18:21], v[10:11], off offset:32
	global_load_dwordx4 v[22:25], v[10:11], off offset:16
	v_lshl_add_u32 v31, v4, 2, 0
; __device__ __forceinline__ int launder_v(int v) { asm volatile("" : "+v"(v)); return v; }
; __device__ __forceinline__ float rsq_(float x) { return 1.0f / sqrtf(x); }
; #define PG8_STAGEB(bufoff, gbase) do { _Pragma("unroll") for (int _i = 0; _i < 2; ++_i) PG8_GL((const char*)(gbase) + voffB[_i], bufoff, _i); } while (0)
; #define PG8_STAGEA(bufoff, ubase, offs, h, kb) do { _Pragma("unroll") for (int _i = 0; _i < 2; ++_i) { \
;         if constexpr (P::GATHER) PG8_GL(S.A + (size_t)(kb) + (offs)[h][_i], bufoff, _i); \
;         else PG8_GL((const char*)(ubase) + (size_t)(h) * hstepA + (size_t)(kb) + voffA[_i], bufoff, _i); } } while (0)
; #define PG8_WAIT_V(n) asm volatile("s_waitcnt vmcnt(" #n ")" ::: "memory")
; #define PG8_BAR __builtin_amdgcn_s_barrier()
; __device__ __forceinline__ LAS float* T0(ldsp tab, int par) { return (LAS float*)(tab) + par * 256; }
; __device__ __forceinline__ LAS float* T1(ldsp tab, int par) { return (LAS float*)(tab + 2048) + par * 256; }
; #define PROB_WS() unsigned char* w_ = ws; asm volatile("" : "+s"(w_))
; template <class P, bool ALIGN_EPI>
; __device__ __forceinline__ void gemm_phase(ldsp lds, ldsp tab, const P& S) {
;     ...
;     S.prepare(cur, 0, tab);
;     PG8_STAGEB(PG8_SB(0, 0), cB); PG8_STAGEB(PG8_SB(0, 1), cB + hstepB); PG8_STAGEA(PG8_SA(0, 0), cA, goc, 0, 0); PG8_STAGEA(PG8_SA(0, 1), cA, goc, 1, 0);
;     if (wr == 1) PG8_BAR;
;     PG8_WAIT_V(2); PG8_BAR;
;     PG8_STAGEB(PG8_SB(1, 0), cB + kstep); PG8_STAGEA(PG8_SA(1, 0), cA, goc, 0, kstep); PG8_STAGEB(PG8_SB(1, 1), cB + hstepB + kstep);
;     PG8_WAIT_V(6); PG8_BAR;
;     __device__ __forceinline__ void prepare(const Unit& u, int par, ldsp tab) const {
;         PROB_WS(); const float* ssqo = (const float*)(w_ + WS_SSQO);
;         const int tid = launder_v(threadIdx.x); if (tid < 256) { const float* p = ssqo + ((size_t)u.pm * 256 + tid) * 16; const f32x4 a = gld4(p), b = gld4(p + 4), c = gld4(p + 8), d = gld4(p + 12);
;             const float sm = ((a[0] + a[1]) + (a[2] + a[3])) + ((b[0] + b[1]) + (b[2] + b[3])), ss = ((c[0] + c[1]) + (c[2] + c[3])) + ((d[0] + d[1]) + (d[2] + d[3]));
;             const float rm = rsq_(sm * (1.0f / 512.0f) + EPS), rsb = rsq_(ss * (1.0f / 512.0f) + EPS);
;             T0(tab, par)[tid] = rsb; T1(tab, par)[tid] = rm / rsb; } }
.LBB0_1263:
	s_or_b64 exec, exec, s[10:11]
	v_bfe_i32 v4, v12, 27, 1
	v_lshlrev_b32_e32 v1, 4, v12
	v_lshrrev_b32_e32 v4, 22, v4
	v_add_u32_e32 v4, v1, v4
	s_add_u32 s52, s6, 0x2c8f4000
	v_and_b32_e32 v4, 0xfffffc00, v4
	s_addc_u32 s53, s7, 0
	s_lshl_b32 s0, s26, 21
	v_sub_u32_e32 v4, v1, v4
	s_add_u32 s0, s6, s0
	v_ashrrev_i32_e32 v2, 31, v12
	v_lshrrev_b32_e32 v5, 4, v4
	s_addc_u32 s1, s7, 0
	v_lshrrev_b32_e32 v2, 26, v2
	v_bitop3_b32 v4, v5, v4, 32 bitop3:0x6c
	s_add_u32 s54, s0, 0x1af4000
	v_add_u32_e32 v2, v12, v2
	v_ashrrev_i32_e32 v6, 31, v4
	s_addc_u32 s55, s1, 0
	s_lshl_b64 s[0:1], s[20:21], 19
	v_ashrrev_i32_e32 v2, 6, v2
	v_lshrrev_b32_e32 v6, 26, v6
	s_add_u32 s0, s52, s0
	v_lshlrev_b32_e32 v5, 3, v2
	v_add_u32_e32 v6, v4, v6
	s_addc_u32 s1, s53, s1
	s_ashr_i32 s23, s22, 31
	v_and_b32_e32 v5, -16, v5
	v_ashrrev_i32_e32 v7, 6, v6
	v_and_b32_e32 v6, 0xc0, v6
	s_lshl_b64 s[10:11], s[22:23], 19
	v_add_u32_e32 v5, v7, v5
	v_sub_u32_e32 v4, v4, v6
	s_add_u32 s38, s54, s10
	v_lshlrev_b32_e32 v2, 5, v2
	v_ashrrev_i16_sdwa v4, v248, sext(v4) dst_sel:DWORD dst_unused:UNUSED_PAD src0_sel:DWORD src1_sel:BYTE_0
	v_lshlrev_b32_e32 v6, 1, v5
	v_lshrrev_b32_e32 v8, 2, v5
	v_and_b32_e32 v7, 3, v7
	s_mov_b32 s10, 0x1fffe0
	v_and_b32_e32 v2, 32, v2
	v_bfe_i32 v4, v4, 0, 16
	v_and_b32_e32 v6, 24, v6
	v_and_b32_e32 v8, 4, v8
	v_and_or_b32 v7, v5, s10, v7
	v_or3_b32 v6, v7, v8, v6
	v_add_lshl_u32 v4, v2, v4, 1
	v_add_u32_e32 v1, 0x2000, v1
	v_lshl_add_u32 v2, v5, 11, v4
	v_lshl_add_u32 v196, v6, 11, v4
	v_ashrrev_i32_e32 v4, 31, v1
	v_lshrrev_b32_e32 v4, 22, v4
	v_add_u32_e32 v4, v1, v4
	v_ashrrev_i32_e32 v4, 10, v4
	v_mul_i32_i24_e32 v5, 0x400, v4
	v_sub_u32_e32 v1, v1, v5
	v_lshrrev_b32_e32 v5, 4, v1
	v_bitop3_b32 v1, v5, v1, 32 bitop3:0x6c
	v_ashrrev_i32_e32 v6, 31, v1
	v_lshrrev_b32_e32 v6, 26, v6
	v_lshlrev_b32_e32 v5, 3, v4
	v_add_u32_e32 v6, v1, v6
	s_addc_u32 s39, s55, s11
	s_ashr_i32 s3, s2, 6
	v_and_b32_e32 v5, -16, v5
	v_ashrrev_i32_e32 v7, 6, v6
	v_and_b32_e32 v6, 0xc0, v6
	v_add_u32_e32 v5, v7, v5
	v_sub_u32_e32 v1, v1, v6
	s_lshl_b32 s23, s3, 10
	v_lshlrev_b32_e32 v4, 5, v4
	v_ashrrev_i16_sdwa v1, v248, sext(v1) dst_sel:DWORD dst_unused:UNUSED_PAD src0_sel:DWORD src1_sel:BYTE_0
	v_lshlrev_b32_e32 v6, 1, v5
	v_lshrrev_b32_e32 v8, 2, v5
	v_and_b32_e32 v7, 3, v7
	s_add_i32 s56, s23, 0
	v_and_b32_e32 v4, 32, v4
	v_bfe_i32 v1, v1, 0, 16
	v_and_b32_e32 v6, 24, v6
	v_and_b32_e32 v8, 4, v8
	v_and_or_b32 v7, v5, s10, v7
	s_add_i32 m0, s56, 0x10000
	v_or3_b32 v6, v7, v8, v6
	v_add_lshl_u32 v1, v4, v1, 1
	s_ashr_i32 s13, s2, 8
	global_load_lds_dwordx4 v196, s[38:39]
	s_add_i32 m0, s56, 0x12000
	v_lshl_add_u32 v200, v6, 11, v1
	s_add_u32 s10, s38, 0x40000
	global_load_lds_dwordx4 v200, s[38:39]
	s_addc_u32 s11, s39, 0
	s_add_i32 m0, s56, 0x14000
	s_add_i32 s57, s56, 0x2000
	global_load_lds_dwordx4 v196, s[10:11]
	s_add_i32 m0, s56, 0x16000
	v_lshl_add_u32 v198, v5, 11, v1
	global_load_lds_dwordx4 v200, s[10:11]
	s_mov_b32 m0, s56
	s_add_u32 s10, s0, 0x40000
	global_load_lds_dwordx4 v2, s[0:1]
	s_mov_b32 m0, s57
	s_addc_u32 s11, s1, 0
	s_add_i32 s58, s56, 0x4000
	global_load_lds_dwordx4 v198, s[0:1]
	s_mov_b32 m0, s58
	s_add_i32 s59, s56, 0x6000
	global_load_lds_dwordx4 v2, s[10:11]
	s_mov_b32 m0, s59
	v_mov_b32_e32 v197, v3
	global_load_lds_dwordx4 v198, s[10:11]
	v_cmp_gt_i32_e32 vcc, 0x100, v0
	s_and_b64 exec, exec, vcc
	s_cbranch_execz .Lprep_outproj_skip
	s_waitcnt vmcnt(8)
	v_add_f32_e32 v1, v26, v27
	v_add_f32_e32 v32, v28, v29
	v_add_f32_e32 v1, v1, v32
	v_add_f32_e32 v32, v22, v23
	v_add_f32_e32 v5, v24, v25
	v_add_f32_e32 v32, v32, v5
	v_add_f32_e32 v1, v1, v32
	v_add_f32_e32 v32, v18, v19
	v_add_f32_e32 v5, v20, v21
	v_add_f32_e32 v32, v32, v5
	v_add_f32_e32 v5, v14, v15
	v_add_f32_e32 v6, v16, v17
	v_add_f32_e32 v5, v5, v6
	v_fmamk_f32 v1, v1, 0x3b000000, v247
	v_add_f32_e32 v32, v32, v5
	v_cmp_gt_f32_e32 vcc, 0xf800000, v1
	v_mul_f32_e32 v5, 0x4f800000, v1
	v_fmamk_f32 v32, v32, 0x3b000000, v247
	v_cndmask_b32_e32 v1, v1, v5, vcc
	v_sqrt_f32_e32 v5, v1
	s_nop 0
	v_add_u32_e32 v6, -1, v5
	v_fma_f32 v7, -v6, v5, v1
	v_cmp_ge_f32_e64 s[10:11], 0, v7
	v_add_u32_e32 v7, 1, v5
	s_nop 0
	v_cndmask_b32_e64 v6, v5, v6, s[10:11]
	v_fma_f32 v5, -v7, v5, v1
	v_cmp_lt_f32_e64 s[10:11], 0, v5
	s_nop 1
	v_cndmask_b32_e64 v5, v6, v7, s[10:11]
	v_mul_f32_e32 v6, 0x37800000, v5
	v_cndmask_b32_e32 v5, v5, v6, vcc
	v_cmp_class_f32_e32 vcc, v1, v242
	s_nop 1
	v_cndmask_b32_e32 v1, v5, v1, vcc
	v_div_scale_f32 v5, s[10:11], v1, v1, 1.0
	v_rcp_f32_e32 v6, v5
	s_nop 0
	v_fma_f32 v7, -v5, v6, 1.0
	v_fmac_f32_e32 v6, v7, v6
	v_div_scale_f32 v7, vcc, 1.0, v1, 1.0
	v_mul_f32_e32 v8, v7, v6
	v_fma_f32 v9, -v5, v8, v7
	v_fmac_f32_e32 v8, v9, v6
	v_fma_f32 v5, -v5, v8, v7
	v_div_fmas_f32 v5, v5, v6, v8
	v_div_fixup_f32 v1, v5, v1, 1.0
	v_cmp_gt_f32_e32 vcc, 0xf800000, v32
	v_mul_f32_e32 v5, 0x4f800000, v32
	s_nop 0
	v_cndmask_b32_e32 v32, v32, v5, vcc
	v_sqrt_f32_e32 v5, v32
	s_nop 0
	v_add_u32_e32 v6, -1, v5
	v_fma_f32 v7, -v6, v5, v32
	v_cmp_ge_f32_e64 s[10:11], 0, v7
	v_add_u32_e32 v7, 1, v5
	s_nop 0
	v_cndmask_b32_e64 v6, v5, v6, s[10:11]
	v_fma_f32 v5, -v7, v5, v32
	v_cmp_lt_f32_e64 s[10:11], 0, v5
	s_nop 1
	v_cndmask_b32_e64 v5, v6, v7, s[10:11]
	v_mul_f32_e32 v6, 0x37800000, v5
	v_cndmask_b32_e32 v5, v5, v6, vcc
	v_cmp_class_f32_e32 vcc, v32, v242
	s_nop 1
	v_cndmask_b32_e32 v32, v5, v32, vcc
	v_div_scale_f32 v5, s[10:11], v32, v32, 1.0
	v_rcp_f32_e32 v6, v5
	s_nop 0
	v_fma_f32 v7, -v5, v6, 1.0
	v_fmac_f32_e32 v6, v7, v6
	v_div_scale_f32 v7, vcc, 1.0, v32, 1.0
	v_mul_f32_e32 v8, v7, v6
	v_fma_f32 v9, -v5, v8, v7
	v_fmac_f32_e32 v8, v9, v6
	v_fma_f32 v5, -v5, v8, v7
	v_div_fmas_f32 v5, v5, v6, v8
	v_div_fixup_f32 v32, v5, v32, 1.0
	v_add_u32_e32 v5, 0x20000, v31
	ds_write_b32 v5, v32
	v_div_scale_f32 v5, s[10:11], v32, v32, v1
	v_rcp_f32_e32 v6, v5
	s_nop 0
	v_fma_f32 v7, -v5, v6, 1.0
	v_fmac_f32_e32 v6, v7, v6
	v_div_scale_f32 v7, vcc, v1, v32, v1
	v_mul_f32_e32 v8, v7, v6
	v_fma_f32 v9, -v5, v8, v7
	v_fmac_f32_e32 v8, v9, v6
	v_fma_f32 v5, -v5, v8, v7
	v_div_fmas_f32 v5, v5, v6, v8
	v_div_fixup_f32 v1, v5, v32, v1
	v_add_u32_e32 v32, 0x20800, v31
	ds_write_b32 v32, v1
.Lprep_outproj_skip:
	s_mov_b64 exec, -1
	v_mov_b32_e32 v201, v3
	v_mov_b32_e32 v199, v3
	s_cmp_eq_u32 s13, 1
	v_mov_b64_e32 v[240:241], 0x100
	v_lshl_add_u64 v[10:11], s[38:39], 0, v[196:197]
	s_waitcnt vmcnt(0)
	v_lshl_add_u64 v[8:9], s[38:39], 0, v[200:201]
	v_lshl_add_u64 v[4:5], s[0:1], 0, v[2:3]
	s_cselect_b64 s[10:11], -1, 0
	s_cmp_lg_u32 s13, 1
	v_lshl_add_u64 v[6:7], s[0:1], 0, v[198:199]
	s_cbranch_scc1 .LBB0_1265
	s_barrier
